# q/k/v projection epilogue publishes its 16-byte row stores write-through (sc1) so the chip-level barrier after it has nothing left to write back; on top of the arrival-time L1 invalidate
# baseline (speedup 1.0000x reference)
; __device__ __forceinline__ unsigned cvt_pk_bf16(float lo, float hi) { unsigned r; asm volatile("v_cvt_pk_bf16_f32 %0, %1, %2" : "=v"(r) : "v"(lo), "v"(hi)); return r; }
; #define NEXT_ROW(roff, m, LD) do { roff += (size_t)((m) == 3 ? 80 : 16) * (LD); asm volatile("" : "+v"(roff) :: "memory"); } while (0)
;     __device__ __forceinline__ void operator()(Acc& acc, const Unit& u, int wr, int wc, int fr, int fq, LAS unsigned char* le, int wid, int lane, int& cpm) const {
;     ...
;         size_t roff = (size_t)(row0 + wr * 64 + fr) * NQKV + u.pn * 256 + wc * 32 + fq * 8;
; #pragma unroll
;         for (int ai = 0; ai < 2; ++ai)
; #pragma unroll
;             for (int m = 0; m < 4; ++m) { bf16* rowp = out + roff;
; #pragma unroll
;                 for (int bj = 0; bj < 2; ++bj) { const f32x4 v0 = acc[ai][bj][m][0], v1 = acc[ai][bj][m][1];
;                     u32x4 w; w.x = cvt_pk_bf16(v0[0], v0[1]); w.y = cvt_pk_bf16(v0[2], v0[3]); w.z = cvt_pk_bf16(v1[0], v1[1]); w.w = cvt_pk_bf16(v1[2], v1[3]);
;                     ST_NT((u32x4*)(rowp + bj * 128), w); }
;                 NEXT_ROW(roff, m, NQKV); }
.LBB0_378:
	s_lshl_b32 s14, s24, 8
	s_ashr_i32 s15, s14, 31
	v_add_u32_e32 v130, s52, v193
	v_lshl_add_u64 v[128:129], v[158:159], 0, s[14:15]
	s_movk_i32 s3, 0x1800
	v_mad_i64_i32 v[128:129], s[14:15], v130, s3, v[128:129]
	v_lshl_add_u64 v[130:131], v[128:129], 1, s[18:19]
	v_cvt_pk_bf16_f32 v80, v80, v81
	v_cvt_pk_bf16_f32 v81, v82, v83
	v_cvt_pk_bf16_f32 v82, v92, v93
	v_cvt_pk_bf16_f32 v83, v94, v95
	global_store_dwordx4 v[130:131], v[80:83], off sc1
	s_andn2_b64 vcc, exec, s[46:47]
	s_mov_b64 s[14:15], -1
	v_cvt_pk_bf16_f32 v80, v120, v121
	v_cvt_pk_bf16_f32 v81, v122, v123
	v_cvt_pk_bf16_f32 v82, v124, v125
	v_cvt_pk_bf16_f32 v83, v126, v127
	global_store_dwordx4 v[130:131], v[80:83], off offset:256 sc1
	s_nop 1
	v_lshl_add_u64 v[80:81], v[128:129], 0, s[40:41]
	v_cvt_pk_bf16_f32 v52, v52, v53
	v_cvt_pk_bf16_f32 v53, v54, v55
	v_cvt_pk_bf16_f32 v54, v68, v69
	v_cvt_pk_bf16_f32 v55, v70, v71
	s_nop 0
	v_lshl_add_u64 v[82:83], v[80:81], 1, s[18:19]
	global_store_dwordx4 v[82:83], v[52:55], off sc1
	s_nop 1
	v_cvt_pk_bf16_f32 v52, v104, v105
	v_cvt_pk_bf16_f32 v53, v106, v107
	v_cvt_pk_bf16_f32 v54, v112, v113
	v_cvt_pk_bf16_f32 v55, v114, v115
	global_store_dwordx4 v[82:83], v[52:55], off offset:256 sc1
	s_nop 1
	v_lshl_add_u64 v[52:53], v[80:81], 0, s[40:41]
	v_cvt_pk_bf16_f32 v28, v28, v29
	v_cvt_pk_bf16_f32 v29, v30, v31
	v_cvt_pk_bf16_f32 v30, v36, v37
	v_cvt_pk_bf16_f32 v31, v38, v39
	s_nop 0
	v_lshl_add_u64 v[54:55], v[52:53], 1, s[18:19]
	global_store_dwordx4 v[54:55], v[28:31], off sc1
	s_nop 1
	v_cvt_pk_bf16_f32 v28, v84, v85
	v_cvt_pk_bf16_f32 v29, v86, v87
	v_cvt_pk_bf16_f32 v30, v96, v97
	v_cvt_pk_bf16_f32 v31, v98, v99
	global_store_dwordx4 v[54:55], v[28:31], off offset:256 sc1
	s_nop 1
	v_lshl_add_u64 v[28:29], v[52:53], 0, s[40:41]
	v_cvt_pk_bf16_f32 v8, v8, v9
	v_cvt_pk_bf16_f32 v9, v10, v11
	v_cvt_pk_bf16_f32 v10, v16, v17
	v_cvt_pk_bf16_f32 v11, v18, v19
	s_nop 0
	v_lshl_add_u64 v[30:31], v[28:29], 1, s[18:19]
	global_store_dwordx4 v[30:31], v[8:11], off sc1
	v_lshl_add_u64 v[16:17], v[28:29], 0, s[42:43]
	s_nop 0
	v_cvt_pk_bf16_f32 v8, v48, v49
	v_cvt_pk_bf16_f32 v9, v50, v51
	v_cvt_pk_bf16_f32 v10, v64, v65
	v_cvt_pk_bf16_f32 v11, v66, v67
	global_store_dwordx4 v[30:31], v[8:11], off offset:256 sc1
	s_nop 0
	v_lshl_add_u64 v[18:19], v[16:17], 1, s[18:19]
	v_cvt_pk_bf16_f32 v8, v56, v57
	v_cvt_pk_bf16_f32 v9, v58, v59
	v_cvt_pk_bf16_f32 v10, v72, v73
	v_cvt_pk_bf16_f32 v11, v74, v75
	global_store_dwordx4 v[18:19], v[8:11], off sc1
	v_lshl_add_u64 v[16:17], v[16:17], 0, s[40:41]
	s_nop 0
	v_cvt_pk_bf16_f32 v8, v108, v109
	v_cvt_pk_bf16_f32 v9, v110, v111
	v_cvt_pk_bf16_f32 v10, v116, v117
	v_cvt_pk_bf16_f32 v11, v118, v119
	global_store_dwordx4 v[18:19], v[8:11], off offset:256 sc1
	s_nop 0
	v_lshl_add_u64 v[18:19], v[16:17], 1, s[18:19]
	v_cvt_pk_bf16_f32 v8, v32, v33
	v_cvt_pk_bf16_f32 v9, v34, v35
	v_cvt_pk_bf16_f32 v10, v40, v41
	v_cvt_pk_bf16_f32 v11, v42, v43
	global_store_dwordx4 v[18:19], v[8:11], off sc1
	v_lshl_add_u64 v[16:17], v[16:17], 0, s[40:41]
	s_nop 0
	v_cvt_pk_bf16_f32 v8, v88, v89
	v_cvt_pk_bf16_f32 v9, v90, v91
	v_cvt_pk_bf16_f32 v10, v100, v101
	v_cvt_pk_bf16_f32 v11, v102, v103
	global_store_dwordx4 v[18:19], v[8:11], off offset:256 sc1
	s_nop 0
	v_lshl_add_u64 v[18:19], v[16:17], 1, s[18:19]
	v_cvt_pk_bf16_f32 v8, v12, v13
	v_cvt_pk_bf16_f32 v9, v14, v15
	v_cvt_pk_bf16_f32 v10, v20, v21
	v_cvt_pk_bf16_f32 v11, v22, v23
	global_store_dwordx4 v[18:19], v[8:11], off sc1
	s_nop 1
	v_cvt_pk_bf16_f32 v8, v60, v61
	v_cvt_pk_bf16_f32 v9, v62, v63
	v_cvt_pk_bf16_f32 v10, v76, v77
	v_cvt_pk_bf16_f32 v11, v78, v79
	global_store_dwordx4 v[18:19], v[8:11], off offset:256 sc1
	s_nop 1
	v_lshl_add_u64 v[8:9], v[16:17], 0, s[40:41]
	v_cvt_pk_bf16_f32 v0, v0, v1
	v_cvt_pk_bf16_f32 v1, v2, v3
	v_cvt_pk_bf16_f32 v2, v4, v5
	v_cvt_pk_bf16_f32 v3, v6, v7
	s_nop 0
	v_lshl_add_u64 v[10:11], v[8:9], 1, s[18:19]
	global_store_dwordx4 v[10:11], v[0:3], off sc1
	s_nop 1
	v_cvt_pk_bf16_f32 v0, v24, v25
	v_cvt_pk_bf16_f32 v1, v26, v27
	v_cvt_pk_bf16_f32 v2, v44, v45
	v_cvt_pk_bf16_f32 v3, v46, v47
	global_store_dwordx4 v[10:11], v[0:3], off offset:256 sc1
	s_nop 1
	v_lshl_add_u64 v[0:1], v[8:9], 0, s[42:43]
	s_cbranch_vccnz .LBB0_257
	s_and_b64 vcc, exec, s[4:5]
	s_cbranch_vccnz .LBB0_256
	s_barrier
	s_branch .LBB0_256
